# LSTM layer 2: bias kept in registers as the MFMA C operand; the hn1 and skip-feature half of the fused FC head plus every kernarg and weight fetch moved into the prologue
# speedup vs baseline: 1.0115x; 1.0082x over previous
_Z6k_lstmILi128ELi8ELb0ELb1EEvPKDF16_S1_S1_PKfPDF16_S1_S1_S1_S3_S3_S3_PfS5_:
	s_load_dwordx4 s[4:7], s[0:1], 0x10
	s_load_dwordx2 s[8:9], s[0:1], 0x0
	s_load_dwordx2 s[26:27], s[0:1], 0x38
	s_load_dwordx2 s[28:29], s[0:1], 0x40
	s_load_dwordx2 s[30:31], s[0:1], 0x48
	s_load_dwordx2 s[32:33], s[0:1], 0x50
	s_load_dwordx2 s[34:35], s[0:1], 0x58
	s_load_dwordx2 s[36:37], s[0:1], 0x60
	v_and_b32_e32 v1, 63, v0
	v_lshrrev_b32_e32 v221, 6, v0
	v_lshlrev_b32_e32 v222, 15, v221
	v_lshl_add_u32 v222, v1, 4, v222
	v_readfirstlane_b32 s24, v221
	s_waitcnt lgkmcnt(0)
	v_add_u32_e32 v1, 0x0, v222
	global_load_dwordx4 v[2:5], v1, s[4:5] offset:0
	global_load_dwordx4 v[6:9], v1, s[4:5] offset:1024
	global_load_dwordx4 v[10:13], v1, s[4:5] offset:2048
	global_load_dwordx4 v[14:17], v1, s[4:5] offset:3072
	v_add_u32_e32 v1, 0x1000, v222
	global_load_dwordx4 v[18:21], v1, s[4:5] offset:0
	global_load_dwordx4 v[22:25], v1, s[4:5] offset:1024
	global_load_dwordx4 v[26:29], v1, s[4:5] offset:2048
	global_load_dwordx4 v[30:33], v1, s[4:5] offset:3072
	v_add_u32_e32 v1, 0x2000, v222
	global_load_dwordx4 v[34:37], v1, s[4:5] offset:0
	global_load_dwordx4 v[38:41], v1, s[4:5] offset:1024
	global_load_dwordx4 v[42:45], v1, s[4:5] offset:2048
	global_load_dwordx4 v[46:49], v1, s[4:5] offset:3072
	v_add_u32_e32 v1, 0x3000, v222
	global_load_dwordx4 v[50:53], v1, s[4:5] offset:0
	global_load_dwordx4 v[54:57], v1, s[4:5] offset:1024
	global_load_dwordx4 v[58:61], v1, s[4:5] offset:2048
	global_load_dwordx4 v[62:65], v1, s[4:5] offset:3072
	v_add_u32_e32 v1, 0x4000, v222
	global_load_dwordx4 v[66:69], v1, s[4:5] offset:0
	global_load_dwordx4 v[70:73], v1, s[4:5] offset:1024
	global_load_dwordx4 v[74:77], v1, s[4:5] offset:2048
	global_load_dwordx4 v[78:81], v1, s[4:5] offset:3072
	v_add_u32_e32 v1, 0x5000, v222
	global_load_dwordx4 v[82:85], v1, s[4:5] offset:0
	global_load_dwordx4 v[86:89], v1, s[4:5] offset:1024
	global_load_dwordx4 v[90:93], v1, s[4:5] offset:2048
	global_load_dwordx4 v[94:97], v1, s[4:5] offset:3072
	v_add_u32_e32 v1, 0x6000, v222
	global_load_dwordx4 v[98:101], v1, s[4:5] offset:0
	global_load_dwordx4 v[102:105], v1, s[4:5] offset:1024
	global_load_dwordx4 v[106:109], v1, s[4:5] offset:2048
	global_load_dwordx4 v[110:113], v1, s[4:5] offset:3072
	v_add_u32_e32 v1, 0x7000, v222
	global_load_dwordx4 v[114:117], v1, s[4:5] offset:0
	global_load_dwordx4 v[118:121], v1, s[4:5] offset:1024
	global_load_dwordx4 v[122:125], v1, s[4:5] offset:2048
	global_load_dwordx4 v[126:129], v1, s[4:5] offset:3072
	v_and_b32_e32 v1, 63, v0
	v_lshlrev_b32_e32 v1, 4, v1
	v_lshl_add_u32 v1, v221, 10, v1
	global_load_dwordx4 v[142:145], v1, s[26:27]
	v_add_u32_e32 v1, 0x2000, v1
	global_load_dwordx4 v[146:149], v1, s[26:27]
	v_add_u32_e32 v1, 0x2000, v1
	global_load_dwordx4 v[150:153], v1, s[26:27]
	v_add_u32_e32 v1, 0x2000, v1
	global_load_dwordx4 v[154:157], v1, s[26:27]
	v_add_u32_e32 v1, 0x2000, v1
	global_load_dwordx4 v[238:241], v1, s[26:27]
	v_add_u32_e32 v1, 0x2000, v1
	global_load_dwordx4 v[242:245], v1, s[26:27]
	v_add_u32_e32 v1, 0x2000, v1
	global_load_dwordx4 v[246:249], v1, s[26:27]
	v_add_u32_e32 v1, 0x2000, v1
	global_load_dwordx4 v[250:253], v1, s[26:27]
	v_lshlrev_b32_e32 v1, 2, v0
	global_load_dword v174, v1, s[6:7]
	v_add_u32_e32 v213, 0xf000, v1
	s_mul_i32 s22, s2, 48
	v_lshrrev_b32_e32 v1, 4, v0
	v_and_b32_e32 v221, 15, v0
	v_lshlrev_b32_e32 v221, 4, v221
	v_add_u32_e32 v222, s22, v1
	v_min_u32_e32 v214, 0x270f, v222
	v_lshl_add_u32 v214, v214, 8, v221
	v_add_u32_e32 v222, 16, v222
	v_min_u32_e32 v215, 0x270f, v222
	v_lshl_add_u32 v215, v215, 8, v221
	v_add_u32_e32 v222, 16, v222
	v_min_u32_e32 v216, 0x270f, v222
	v_lshl_add_u32 v216, v216, 8, v221
	v_mul_u32_u24_e32 v217, 0x50, v1
	v_and_b32_e32 v221, 3, v0
	v_mul_u32_u24_e32 v221, 0xf00, v221
	v_bfe_u32 v222, v0, 2, 2
	v_lshl_add_u32 v221, v222, 4, v221
	v_add_u32_e32 v217, v217, v221
	s_add_u32 s12, s8, 0x271000
	s_addc_u32 s13, s9, 0
	s_add_u32 s10, s8, 0x249f000
	s_addc_u32 s11, s9, 0
	global_load_dwordx4 v[186:189], v214, s[8:9]
	global_load_dwordx4 v[190:193], v215, s[8:9]
	global_load_dwordx4 v[178:181], v214, s[12:13]
	global_load_dwordx4 v[182:185], v214, s[10:11]
	global_load_dwordx4 v[162:165], v216, s[10:11]
	s_add_u32 s8, s8, 0x271000
	s_addc_u32 s9, s9, 0
	s_add_u32 s12, s12, 0x271000
	s_addc_u32 s13, s13, 0
	v_and_b32_e32 v1, 15, v0
	v_bfe_u32 v221, v0, 4, 2
	v_mul_u32_u24_e32 v210, 0x50, v1
	v_mul_u32_u24_e32 v222, 0xf00, v221
	v_add_u32_e32 v210, v210, v222
	v_add_u32_e32 v211, 0x7800, v210
	v_add_u32_e32 v223, 0xf800, v210
	v_lshrrev_b32_e32 v222, 6, v0
	v_lshrrev_b32_e32 v212, 1, v221
	v_and_b32_e32 v220, 1, v222
	v_lshl_add_u32 v212, v220, 1, v212
	v_mul_u32_u24_e32 v212, 0xf00, v212
	v_mul_u32_u24_e32 v220, 0x50, v1
	v_add_u32_e32 v212, v212, v220
	v_add_u32_e32 v212, 0x7800, v212
	v_lshrrev_b32_e32 v220, 1, v222
	v_lshl_add_u32 v212, v220, 4, v212
	v_and_b32_e32 v220, 1, v221
	v_lshl_add_u32 v212, v220, 3, v212
	v_lshl_add_u32 v224, v222, 2, v221
	v_lshlrev_b32_e32 v224, 2, v224
	v_lshl_add_u32 v224, v1, 7, v224
	v_add_u32_e32 v224, 0x13400, v224
	v_lshl_add_u32 v130, v222, 2, v221
	v_lshlrev_b32_e32 v130, 4, v130
	v_add_u32_e32 v131, s22, v1
	v_min_u32_e32 v132, 0x270f, v131
	v_lshl_add_u32 v132, v132, 9, v130
	global_load_dwordx4 v[226:229], v132, s[36:37]
	v_add_u32_e32 v131, 16, v131
	v_min_u32_e32 v132, 0x270f, v131
	v_lshl_add_u32 v132, v132, 9, v130
	global_load_dwordx4 v[230:233], v132, s[36:37]
	v_add_u32_e32 v131, 16, v131
	v_min_u32_e32 v132, 0x270f, v131
	v_lshl_add_u32 v132, v132, 9, v130
	global_load_dwordx4 v[234:237], v132, s[36:37]
	v_mov_b32_e32 v158, 0
	v_mov_b32_e32 v159, 0
	v_mov_b32_e32 v160, 0
	v_mov_b32_e32 v161, 0
	v_mov_b32_e32 v130, 0
	v_mov_b32_e32 v131, 0
	v_mov_b32_e32 v132, 0
	v_mov_b32_e32 v133, 0
	v_mov_b32_e32 v134, 0
	v_mov_b32_e32 v135, 0
	v_mov_b32_e32 v136, 0
	v_mov_b32_e32 v137, 0
	v_mov_b32_e32 v138, 0
	v_mov_b32_e32 v139, 0
	v_mov_b32_e32 v140, 0
	v_mov_b32_e32 v141, 0
	v_mov_b32_e32 v220, 0x4038aa3b
	s_mov_b32 s16, 0xc0b8aa3b
	v_lshlrev_b32_e32 v1, 4, v0
	v_add_u32_e32 v1, 0x7800, v1
	ds_write_b128 v1, v[158:161]
	ds_write_b128 v1, v[158:161] offset:8192
	s_waitcnt vmcnt(0)
	ds_write_b32 v213, v174
	ds_write_b128 v217, v[190:193] offset:1280
	ds_write_b128 v217, v[182:185] offset:63488
	s_cmp_ge_u32 s24, 4
	s_cbranch_scc1 .Ll2_pro_skip
	ds_write_b128 v217, v[186:189]
	ds_write_b128 v217, v[178:181] offset:15360
	v_add_u32_e32 v1, 0xa00, v217
	ds_write_b128 v1, v[162:165] offset:63488
.Ll2_pro_skip:
	v_lshrrev_b32_e32 v222, 6, v0
	v_lshlrev_b32_e32 v213, 6, v222
	v_lshl_add_u32 v213, v221, 4, v213
	v_add_u32_e32 v213, 0xf000, v213
	s_waitcnt lgkmcnt(0)
	s_barrier
	ds_read_b128 v[174:177], v223 offset:0
	ds_read_b128 v[178:181], v223 offset:1280
	ds_read_b128 v[182:185], v223 offset:2560
	s_waitcnt lgkmcnt(2)
	v_mfma_f32_16x16x32_f16 v[226:229], v[142:145], v[174:177], v[226:229]
	ds_read_b128 v[174:177], v223 offset:16
	s_waitcnt lgkmcnt(2)
	v_mfma_f32_16x16x32_f16 v[230:233], v[142:145], v[178:181], v[230:233]
	ds_read_b128 v[178:181], v223 offset:1296
	s_waitcnt lgkmcnt(2)
	v_mfma_f32_16x16x32_f16 v[234:237], v[142:145], v[182:185], v[234:237]
	ds_read_b128 v[182:185], v223 offset:2576
	s_waitcnt lgkmcnt(2)
	v_mfma_f32_16x16x32_f16 v[226:229], v[146:149], v[174:177], v[226:229]
	ds_read_b128 v[174:177], v223 offset:32
	s_waitcnt lgkmcnt(2)
	v_mfma_f32_16x16x32_f16 v[230:233], v[146:149], v[178:181], v[230:233]
	ds_read_b128 v[178:181], v223 offset:1312
	s_waitcnt lgkmcnt(2)
	v_mfma_f32_16x16x32_f16 v[234:237], v[146:149], v[182:185], v[234:237]
	ds_read_b128 v[182:185], v223 offset:2592
	s_waitcnt lgkmcnt(2)
	v_mfma_f32_16x16x32_f16 v[226:229], v[150:153], v[174:177], v[226:229]
	ds_read_b128 v[174:177], v223 offset:48
	s_waitcnt lgkmcnt(2)
	v_mfma_f32_16x16x32_f16 v[230:233], v[150:153], v[178:181], v[230:233]
	ds_read_b128 v[178:181], v223 offset:1328
	s_waitcnt lgkmcnt(2)
	v_mfma_f32_16x16x32_f16 v[234:237], v[150:153], v[182:185], v[234:237]
	ds_read_b128 v[182:185], v223 offset:2608
	s_waitcnt lgkmcnt(2)
	v_mfma_f32_16x16x32_f16 v[226:229], v[154:157], v[174:177], v[226:229]
	s_waitcnt lgkmcnt(1)
	v_mfma_f32_16x16x32_f16 v[230:233], v[154:157], v[178:181], v[230:233]
	s_waitcnt lgkmcnt(0)
	v_mfma_f32_16x16x32_f16 v[234:237], v[154:157], v[182:185], v[234:237]
	ds_read_b128 v[194:197], v213 offset:0
	ds_read_b128 v[198:201], v213 offset:512
	ds_read_b128 v[202:205], v213 offset:1024
	ds_read_b128 v[206:209], v213 offset:1536
	s_waitcnt lgkmcnt(0)
	ds_read_b128 v[174:177], v210 offset:0
	ds_read_b128 v[178:181], v210 offset:16
	s_waitcnt lgkmcnt(1)
	ds_read_b128 v[182:185], v210 offset:32
	v_mfma_f32_16x16x32_f16 v[142:145], v[2:5], v[174:177], v[194:197]
	v_mfma_f32_16x16x32_f16 v[146:149], v[6:9], v[174:177], v[198:201]
	v_mfma_f32_16x16x32_f16 v[150:153], v[10:13], v[174:177], v[202:205]
	v_mfma_f32_16x16x32_f16 v[154:157], v[14:17], v[174:177], v[206:209]
	s_waitcnt lgkmcnt(1)
	ds_read_b128 v[174:177], v210 offset:48
	v_mfma_f32_16x16x32_f16 v[142:145], v[18:21], v[178:181], v[142:145]
	v_mfma_f32_16x16x32_f16 v[146:149], v[22:25], v[178:181], v[146:149]
	v_mfma_f32_16x16x32_f16 v[150:153], v[26:29], v[178:181], v[150:153]
	v_mfma_f32_16x16x32_f16 v[154:157], v[30:33], v[178:181], v[154:157]
	s_waitcnt lgkmcnt(0)
	s_mov_b32 s17, 0
	s_barrier
.Llstm2_loop:
	ds_read_b128 v[178:181], v211 offset:0
	v_mfma_f32_16x16x32_f16 v[142:145], v[34:37], v[182:185], v[142:145]
	v_mfma_f32_16x16x32_f16 v[146:149], v[38:41], v[182:185], v[146:149]
	v_mfma_f32_16x16x32_f16 v[150:153], v[42:45], v[182:185], v[150:153]
	v_mfma_f32_16x16x32_f16 v[154:157], v[46:49], v[182:185], v[154:157]
	ds_read_b128 v[182:185], v211 offset:16
	v_mfma_f32_16x16x32_f16 v[142:145], v[50:53], v[174:177], v[142:145]
	v_mfma_f32_16x16x32_f16 v[146:149], v[54:57], v[174:177], v[146:149]
	v_mfma_f32_16x16x32_f16 v[150:153], v[58:61], v[174:177], v[150:153]
	v_mfma_f32_16x16x32_f16 v[154:157], v[62:65], v[174:177], v[154:157]
	s_cmp_ge_u32 s24, 4
	s_cbranch_scc1 .Lskipx78
	global_load_dwordx4 v[186:189], v214, s[12:13]
.Lskipx78:
	s_waitcnt lgkmcnt(1)
	ds_read_b128 v[174:177], v211 offset:32
	v_mfma_f32_16x16x32_f16 v[142:145], v[66:69], v[178:181], v[142:145]
	v_mfma_f32_16x16x32_f16 v[146:149], v[70:73], v[178:181], v[146:149]
	v_mfma_f32_16x16x32_f16 v[150:153], v[74:77], v[178:181], v[150:153]
	v_mfma_f32_16x16x32_f16 v[154:157], v[78:81], v[178:181], v[154:157]
	global_load_dwordx4 v[190:193], v215, s[8:9]
	s_waitcnt lgkmcnt(1)
	ds_read_b128 v[178:181], v211 offset:48
	v_mfma_f32_16x16x32_f16 v[142:145], v[82:85], v[182:185], v[142:145]
	v_mfma_f32_16x16x32_f16 v[146:149], v[86:89], v[182:185], v[146:149]
	v_mfma_f32_16x16x32_f16 v[150:153], v[90:93], v[182:185], v[150:153]
	v_mfma_f32_16x16x32_f16 v[154:157], v[94:97], v[182:185], v[154:157]
	s_add_u32 s12, s12, 0x271000
	s_waitcnt lgkmcnt(1)
	ds_read_b128 v[182:185], v210 offset:1280
	v_mfma_f32_16x16x32_f16 v[142:145], v[98:101], v[174:177], v[142:145]
	v_mfma_f32_16x16x32_f16 v[146:149], v[102:105], v[174:177], v[146:149]
	v_mfma_f32_16x16x32_f16 v[150:153], v[106:109], v[174:177], v[150:153]
	v_mfma_f32_16x16x32_f16 v[154:157], v[110:113], v[174:177], v[154:157]
	s_addc_u32 s13, s13, 0
	s_waitcnt lgkmcnt(1)
	ds_read_b128 v[174:177], v210 offset:1296
	v_mfma_f32_16x16x32_f16 v[142:145], v[114:117], v[178:181], v[142:145]
	v_mfma_f32_16x16x32_f16 v[146:149], v[118:121], v[178:181], v[146:149]
	s_add_u32 s8, s8, 0x271000
	v_mfma_f32_16x16x32_f16 v[150:153], v[122:125], v[178:181], v[150:153]
	v_mfma_f32_16x16x32_f16 v[154:157], v[126:129], v[178:181], v[154:157]
	s_addc_u32 s9, s9, 0
	s_waitcnt lgkmcnt(1)
	ds_read_b128 v[178:181], v211 offset:1280
	v_mfma_f32_16x16x32_f16 v[158:161], v[2:5], v[182:185], v[194:197]
	v_mfma_f32_16x16x32_f16 v[162:165], v[6:9], v[182:185], v[198:201]
	v_mfma_f32_16x16x32_f16 v[166:169], v[10:13], v[182:185], v[202:205]
	v_mfma_f32_16x16x32_f16 v[170:173], v[14:17], v[182:185], v[206:209]
	s_waitcnt lgkmcnt(1)
	ds_read_b128 v[182:185], v211 offset:1296
	v_mfma_f32_16x16x32_f16 v[158:161], v[18:21], v[174:177], v[158:161]
	v_mfma_f32_16x16x32_f16 v[162:165], v[22:25], v[174:177], v[162:165]
	v_mfma_f32_16x16x32_f16 v[166:169], v[26:29], v[174:177], v[166:169]
	v_mfma_f32_16x16x32_f16 v[170:173], v[30:33], v[174:177], v[170:173]
	v_exp_f32_e32 v142, v142
	v_exp_f32_e32 v143, v143
	v_exp_f32_e32 v144, v144
	v_exp_f32_e32 v145, v145
	v_exp_f32_e32 v146, v146
	v_exp_f32_e32 v147, v147
	v_exp_f32_e32 v148, v148
	v_exp_f32_e32 v149, v149
	v_exp_f32_e32 v150, v150
	v_exp_f32_e32 v151, v151
	v_exp_f32_e32 v152, v152
	v_exp_f32_e32 v153, v153
	v_exp_f32_e32 v154, v154
	v_exp_f32_e32 v155, v155
	v_exp_f32_e32 v156, v156
	v_exp_f32_e32 v157, v157
	v_add_f32_e32 v150, 1.0, v150
	v_add_f32_e32 v151, 1.0, v151
	v_add_f32_e32 v152, 1.0, v152
	v_add_f32_e32 v153, 1.0, v153
	v_add_f32_e32 v146, 1.0, v146
	v_add_f32_e32 v147, 1.0, v147
	v_add_f32_e32 v148, 1.0, v148
	v_add_f32_e32 v149, 1.0, v149
	v_fma_f32 v142, v142, v150, v150
	v_fma_f32 v143, v143, v151, v151
	v_fma_f32 v144, v144, v152, v152
	v_fma_f32 v145, v145, v153, v153
	v_rcp_f32_e32 v146, v146
	v_rcp_f32_e32 v147, v147
	v_rcp_f32_e32 v148, v148
	v_rcp_f32_e32 v149, v149
	v_fma_f32 v150, v150, v220, s16
	v_fma_f32 v151, v151, v220, s16
	v_fma_f32 v152, v152, v220, s16
	v_fma_f32 v153, v153, v220, s16
	v_rcp_f32_e32 v142, v142
	v_rcp_f32_e32 v143, v143
	v_rcp_f32_e32 v144, v144
	v_rcp_f32_e32 v145, v145
	v_mul_f32_e32 v130, v130, v146
	v_mul_f32_e32 v131, v131, v147
	v_mul_f32_e32 v132, v132, v148
	v_mul_f32_e32 v133, v133, v149
	v_fma_f32 v130, v150, v142, v130
	v_fma_f32 v131, v151, v143, v131
	v_fma_f32 v132, v152, v144, v132
	v_fma_f32 v133, v153, v145, v133
	v_exp_f32_e32 v146, v130
	v_exp_f32_e32 v147, v131
	v_exp_f32_e32 v148, v132
	v_exp_f32_e32 v149, v133
	v_add_f32_e32 v142, 1.0, v146
	v_add_f32_e32 v143, 1.0, v147
	v_add_f32_e32 v144, 1.0, v148
	v_add_f32_e32 v145, 1.0, v149
	v_add_f32_e32 v150, -1.0, v146
	v_add_f32_e32 v151, -1.0, v147
	v_add_f32_e32 v152, -1.0, v148
	v_add_f32_e32 v153, -1.0, v149
	v_fma_f32 v154, v154, v142, v142
	v_fma_f32 v155, v155, v143, v143
	v_fma_f32 v156, v156, v144, v144
	v_fma_f32 v157, v157, v145, v145
	v_rcp_f32_e32 v154, v154
	v_rcp_f32_e32 v155, v155
	v_rcp_f32_e32 v156, v156
	v_rcp_f32_e32 v157, v157
	v_mul_f32_e32 v154, v150, v154
	v_mul_f32_e32 v155, v151, v155
	v_mul_f32_e32 v156, v152, v156
	v_mul_f32_e32 v157, v153, v157
	v_cvt_pk_f16_f32 v154, v154, v155
	v_cvt_pk_f16_f32 v155, v156, v157
	ds_write_b64 v212, v[154:155] offset:15360
	s_waitcnt lgkmcnt(2)
	ds_read_b128 v[174:177], v210 offset:1312
	v_mfma_f32_16x16x32_f16 v[158:161], v[66:69], v[178:181], v[158:161]
	v_mfma_f32_16x16x32_f16 v[162:165], v[70:73], v[178:181], v[162:165]
	v_mfma_f32_16x16x32_f16 v[166:169], v[74:77], v[178:181], v[166:169]
	v_mfma_f32_16x16x32_f16 v[170:173], v[78:81], v[178:181], v[170:173]
	s_waitcnt lgkmcnt(2)
	ds_read_b128 v[178:181], v210 offset:1328
	v_mfma_f32_16x16x32_f16 v[158:161], v[82:85], v[182:185], v[158:161]
	v_mfma_f32_16x16x32_f16 v[162:165], v[86:89], v[182:185], v[162:165]
	v_mfma_f32_16x16x32_f16 v[166:169], v[90:93], v[182:185], v[166:169]
	v_mfma_f32_16x16x32_f16 v[170:173], v[94:97], v[182:185], v[170:173]
	s_waitcnt lgkmcnt(1)
	ds_read_b128 v[182:185], v211 offset:1312
	v_mfma_f32_16x16x32_f16 v[158:161], v[34:37], v[174:177], v[158:161]
	v_mfma_f32_16x16x32_f16 v[162:165], v[38:41], v[174:177], v[162:165]
	v_mfma_f32_16x16x32_f16 v[166:169], v[42:45], v[174:177], v[166:169]
	v_mfma_f32_16x16x32_f16 v[170:173], v[46:49], v[174:177], v[170:173]
	s_waitcnt lgkmcnt(1)
	ds_read_b128 v[174:177], v211 offset:1328
	v_mfma_f32_16x16x32_f16 v[158:161], v[50:53], v[178:181], v[158:161]
	v_mfma_f32_16x16x32_f16 v[162:165], v[54:57], v[178:181], v[162:165]
	v_mfma_f32_16x16x32_f16 v[166:169], v[58:61], v[178:181], v[166:169]
	v_mfma_f32_16x16x32_f16 v[170:173], v[62:65], v[178:181], v[170:173]
	s_waitcnt vmcnt(0)
	s_cmp_ge_u32 s24, 4
	s_cbranch_scc1 .Lskips79
	ds_write_b128 v217, v[186:189] offset:0
.Lskips79:
	ds_write_b128 v217, v[190:193] offset:16640
	s_waitcnt lgkmcnt(3)
	ds_read_b128 v[178:181], v210 offset:2560
	v_mfma_f32_16x16x32_f16 v[158:161], v[98:101], v[182:185], v[158:161]
	v_mfma_f32_16x16x32_f16 v[162:165], v[102:105], v[182:185], v[162:165]
	v_mfma_f32_16x16x32_f16 v[166:169], v[106:109], v[182:185], v[166:169]
	v_mfma_f32_16x16x32_f16 v[170:173], v[110:113], v[182:185], v[170:173]
	s_waitcnt lgkmcnt(3)
	ds_read_b128 v[182:185], v210 offset:2576
	v_mfma_f32_16x16x32_f16 v[158:161], v[114:117], v[174:177], v[158:161]
	v_mfma_f32_16x16x32_f16 v[162:165], v[118:121], v[174:177], v[162:165]
	v_mfma_f32_16x16x32_f16 v[166:169], v[122:125], v[174:177], v[166:169]
	v_mfma_f32_16x16x32_f16 v[170:173], v[126:129], v[174:177], v[170:173]
	s_waitcnt lgkmcnt(1)
	ds_read_b128 v[174:177], v211 offset:2560
	v_mfma_f32_16x16x32_f16 v[142:145], v[2:5], v[178:181], v[194:197]
	v_mfma_f32_16x16x32_f16 v[146:149], v[6:9], v[178:181], v[198:201]
	v_mfma_f32_16x16x32_f16 v[150:153], v[10:13], v[178:181], v[202:205]
	v_mfma_f32_16x16x32_f16 v[154:157], v[14:17], v[178:181], v[206:209]
	s_waitcnt lgkmcnt(1)
	ds_read_b128 v[178:181], v211 offset:2576
	v_mfma_f32_16x16x32_f16 v[142:145], v[18:21], v[182:185], v[142:145]
	v_mfma_f32_16x16x32_f16 v[146:149], v[22:25], v[182:185], v[146:149]
	v_mfma_f32_16x16x32_f16 v[150:153], v[26:29], v[182:185], v[150:153]
	v_mfma_f32_16x16x32_f16 v[154:157], v[30:33], v[182:185], v[154:157]
	v_exp_f32_e32 v158, v158
	v_exp_f32_e32 v159, v159
	v_exp_f32_e32 v160, v160
	v_exp_f32_e32 v161, v161
	v_exp_f32_e32 v162, v162
	v_exp_f32_e32 v163, v163
	v_exp_f32_e32 v164, v164
	v_exp_f32_e32 v165, v165
	v_exp_f32_e32 v166, v166
	v_exp_f32_e32 v167, v167
	v_exp_f32_e32 v168, v168
	v_exp_f32_e32 v169, v169
	v_exp_f32_e32 v170, v170
	v_exp_f32_e32 v171, v171
	v_exp_f32_e32 v172, v172
	v_exp_f32_e32 v173, v173
	v_add_f32_e32 v166, 1.0, v166
	v_add_f32_e32 v167, 1.0, v167
	v_add_f32_e32 v168, 1.0, v168
	v_add_f32_e32 v169, 1.0, v169
	v_add_f32_e32 v162, 1.0, v162
	v_add_f32_e32 v163, 1.0, v163
	v_add_f32_e32 v164, 1.0, v164
	v_add_f32_e32 v165, 1.0, v165
	v_fma_f32 v158, v158, v166, v166
	v_fma_f32 v159, v159, v167, v167
	v_fma_f32 v160, v160, v168, v168
	v_fma_f32 v161, v161, v169, v169
	v_rcp_f32_e32 v162, v162
	v_rcp_f32_e32 v163, v163
	v_rcp_f32_e32 v164, v164
	v_rcp_f32_e32 v165, v165
	v_fma_f32 v166, v166, v220, s16
	v_fma_f32 v167, v167, v220, s16
	v_fma_f32 v168, v168, v220, s16
	v_fma_f32 v169, v169, v220, s16
	v_rcp_f32_e32 v158, v158
	v_rcp_f32_e32 v159, v159
	v_rcp_f32_e32 v160, v160
	v_rcp_f32_e32 v161, v161
	v_mul_f32_e32 v134, v134, v162
	v_mul_f32_e32 v135, v135, v163
	v_mul_f32_e32 v136, v136, v164
	v_mul_f32_e32 v137, v137, v165
	v_fma_f32 v134, v166, v158, v134
	v_fma_f32 v135, v167, v159, v135
	v_fma_f32 v136, v168, v160, v136
	v_fma_f32 v137, v169, v161, v137
	v_exp_f32_e32 v162, v134
	v_exp_f32_e32 v163, v135
	v_exp_f32_e32 v164, v136
	v_exp_f32_e32 v165, v137
	v_add_f32_e32 v158, 1.0, v162
	v_add_f32_e32 v159, 1.0, v163
	v_add_f32_e32 v160, 1.0, v164
	v_add_f32_e32 v161, 1.0, v165
	v_add_f32_e32 v166, -1.0, v162
	v_add_f32_e32 v167, -1.0, v163
	v_add_f32_e32 v168, -1.0, v164
	v_add_f32_e32 v169, -1.0, v165
	v_fma_f32 v170, v170, v158, v158
	v_fma_f32 v171, v171, v159, v159
	v_fma_f32 v172, v172, v160, v160
	v_fma_f32 v173, v173, v161, v161
	v_rcp_f32_e32 v170, v170
	v_rcp_f32_e32 v171, v171
	v_rcp_f32_e32 v172, v172
	v_rcp_f32_e32 v173, v173
	v_mul_f32_e32 v170, v166, v170
	v_mul_f32_e32 v171, v167, v171
	v_mul_f32_e32 v172, v168, v172
	v_mul_f32_e32 v173, v169, v173
	v_cvt_pk_f16_f32 v170, v170, v171
	v_cvt_pk_f16_f32 v171, v172, v173
	ds_write_b64 v212, v[170:171] offset:16640
	s_waitcnt lgkmcnt(2)
	ds_read_b128 v[182:185], v210 offset:2592
	v_mfma_f32_16x16x32_f16 v[142:145], v[66:69], v[174:177], v[142:145]
	v_mfma_f32_16x16x32_f16 v[146:149], v[70:73], v[174:177], v[146:149]
	v_mfma_f32_16x16x32_f16 v[150:153], v[74:77], v[174:177], v[150:153]
	v_mfma_f32_16x16x32_f16 v[154:157], v[78:81], v[174:177], v[154:157]
	s_waitcnt lgkmcnt(2)
	ds_read_b128 v[174:177], v210 offset:2608
	v_mfma_f32_16x16x32_f16 v[142:145], v[82:85], v[178:181], v[142:145]
	v_mfma_f32_16x16x32_f16 v[146:149], v[86:89], v[178:181], v[146:149]
	v_mfma_f32_16x16x32_f16 v[150:153], v[90:93], v[178:181], v[150:153]
	v_mfma_f32_16x16x32_f16 v[154:157], v[94:97], v[178:181], v[154:157]
	s_waitcnt lgkmcnt(1)
	ds_read_b128 v[178:181], v211 offset:2592
	v_mfma_f32_16x16x32_f16 v[142:145], v[34:37], v[182:185], v[142:145]
	v_mfma_f32_16x16x32_f16 v[146:149], v[38:41], v[182:185], v[146:149]
	v_mfma_f32_16x16x32_f16 v[150:153], v[42:45], v[182:185], v[150:153]
	v_mfma_f32_16x16x32_f16 v[154:157], v[46:49], v[182:185], v[154:157]
	s_waitcnt lgkmcnt(1)
	ds_read_b128 v[182:185], v211 offset:2608
	v_mfma_f32_16x16x32_f16 v[142:145], v[50:53], v[174:177], v[142:145]
	v_mfma_f32_16x16x32_f16 v[146:149], v[54:57], v[174:177], v[146:149]
	v_mfma_f32_16x16x32_f16 v[150:153], v[58:61], v[174:177], v[150:153]
	v_mfma_f32_16x16x32_f16 v[154:157], v[62:65], v[174:177], v[154:157]
	s_waitcnt lgkmcnt(1)
	ds_read_b128 v[174:177], v210 offset:15360
	v_mfma_f32_16x16x32_f16 v[142:145], v[98:101], v[178:181], v[142:145]
	v_mfma_f32_16x16x32_f16 v[146:149], v[102:105], v[178:181], v[146:149]
	v_mfma_f32_16x16x32_f16 v[150:153], v[106:109], v[178:181], v[150:153]
	v_mfma_f32_16x16x32_f16 v[154:157], v[110:113], v[178:181], v[154:157]
	s_waitcnt lgkmcnt(1)
	ds_read_b128 v[178:181], v210 offset:15376
	v_mfma_f32_16x16x32_f16 v[142:145], v[114:117], v[182:185], v[142:145]
	v_mfma_f32_16x16x32_f16 v[146:149], v[118:121], v[182:185], v[146:149]
	v_mfma_f32_16x16x32_f16 v[150:153], v[122:125], v[182:185], v[150:153]
	v_mfma_f32_16x16x32_f16 v[154:157], v[126:129], v[182:185], v[154:157]
	s_waitcnt lgkmcnt(1)
	ds_read_b128 v[182:185], v210 offset:15392
	v_mfma_f32_16x16x32_f16 v[158:161], v[2:5], v[174:177], v[194:197]
	v_mfma_f32_16x16x32_f16 v[162:165], v[6:9], v[174:177], v[198:201]
	v_mfma_f32_16x16x32_f16 v[166:169], v[10:13], v[174:177], v[202:205]
	v_mfma_f32_16x16x32_f16 v[170:173], v[14:17], v[174:177], v[206:209]
	s_waitcnt lgkmcnt(1)
	ds_read_b128 v[174:177], v210 offset:15408
	v_mfma_f32_16x16x32_f16 v[158:161], v[18:21], v[178:181], v[158:161]
	v_mfma_f32_16x16x32_f16 v[162:165], v[22:25], v[178:181], v[162:165]
	v_mfma_f32_16x16x32_f16 v[166:169], v[26:29], v[178:181], v[166:169]
	v_mfma_f32_16x16x32_f16 v[170:173], v[30:33], v[178:181], v[170:173]
	v_exp_f32_e32 v142, v142
	v_exp_f32_e32 v143, v143
	v_exp_f32_e32 v144, v144
	v_exp_f32_e32 v145, v145
	v_exp_f32_e32 v146, v146
	v_exp_f32_e32 v147, v147
	v_exp_f32_e32 v148, v148
	v_exp_f32_e32 v149, v149
	v_exp_f32_e32 v150, v150
	v_exp_f32_e32 v151, v151
	v_exp_f32_e32 v152, v152
	v_exp_f32_e32 v153, v153
	v_exp_f32_e32 v154, v154
	v_exp_f32_e32 v155, v155
	v_exp_f32_e32 v156, v156
	v_exp_f32_e32 v157, v157
	v_add_f32_e32 v150, 1.0, v150
	v_add_f32_e32 v151, 1.0, v151
	v_add_f32_e32 v152, 1.0, v152
	v_add_f32_e32 v153, 1.0, v153
	v_add_f32_e32 v146, 1.0, v146
	v_add_f32_e32 v147, 1.0, v147
	v_add_f32_e32 v148, 1.0, v148
	v_add_f32_e32 v149, 1.0, v149
	v_fma_f32 v142, v142, v150, v150
	v_fma_f32 v143, v143, v151, v151
	v_fma_f32 v144, v144, v152, v152
	v_fma_f32 v145, v145, v153, v153
	v_rcp_f32_e32 v146, v146
	v_rcp_f32_e32 v147, v147
	v_rcp_f32_e32 v148, v148
	v_rcp_f32_e32 v149, v149
	v_fma_f32 v150, v150, v220, s16
	v_fma_f32 v151, v151, v220, s16
	v_fma_f32 v152, v152, v220, s16
	v_fma_f32 v153, v153, v220, s16
	v_rcp_f32_e32 v142, v142
	v_rcp_f32_e32 v143, v143
	v_rcp_f32_e32 v144, v144
	v_rcp_f32_e32 v145, v145
	v_mul_f32_e32 v138, v138, v146
	v_mul_f32_e32 v139, v139, v147
	v_mul_f32_e32 v140, v140, v148
	v_mul_f32_e32 v141, v141, v149
	v_fma_f32 v138, v150, v142, v138
	v_fma_f32 v139, v151, v143, v139
	v_fma_f32 v140, v152, v144, v140
	v_fma_f32 v141, v153, v145, v141
	v_exp_f32_e32 v146, v138
	v_exp_f32_e32 v147, v139
	v_exp_f32_e32 v148, v140
	v_exp_f32_e32 v149, v141
	v_add_f32_e32 v142, 1.0, v146
	v_add_f32_e32 v143, 1.0, v147
	v_add_f32_e32 v144, 1.0, v148
	v_add_f32_e32 v145, 1.0, v149
	v_add_f32_e32 v150, -1.0, v146
	v_add_f32_e32 v151, -1.0, v147
	v_add_f32_e32 v152, -1.0, v148
	v_add_f32_e32 v153, -1.0, v149
	v_fma_f32 v154, v154, v142, v142
	v_fma_f32 v155, v155, v143, v143
	v_fma_f32 v156, v156, v144, v144
	v_fma_f32 v157, v157, v145, v145
	v_rcp_f32_e32 v154, v154
	v_rcp_f32_e32 v155, v155
	v_rcp_f32_e32 v156, v156
	v_rcp_f32_e32 v157, v157
	v_mul_f32_e32 v154, v150, v154
	v_mul_f32_e32 v155, v151, v155
	v_mul_f32_e32 v156, v152, v156
	v_mul_f32_e32 v157, v153, v157
	v_cvt_pk_f16_f32 v154, v154, v155
	v_cvt_pk_f16_f32 v155, v156, v157
	ds_write_b64 v212, v[154:155] offset:17920
	s_waitcnt lgkmcnt(0)
	s_barrier
	ds_read_b128 v[178:181], v211 offset:15360
	v_mfma_f32_16x16x32_f16 v[158:161], v[34:37], v[182:185], v[158:161]
	v_mfma_f32_16x16x32_f16 v[162:165], v[38:41], v[182:185], v[162:165]
	v_mfma_f32_16x16x32_f16 v[166:169], v[42:45], v[182:185], v[166:169]
	v_mfma_f32_16x16x32_f16 v[170:173], v[46:49], v[182:185], v[170:173]
	ds_read_b128 v[182:185], v211 offset:15376
	v_mfma_f32_16x16x32_f16 v[158:161], v[50:53], v[174:177], v[158:161]
	v_mfma_f32_16x16x32_f16 v[162:165], v[54:57], v[174:177], v[162:165]
	v_mfma_f32_16x16x32_f16 v[166:169], v[58:61], v[174:177], v[166:169]
	v_mfma_f32_16x16x32_f16 v[170:173], v[62:65], v[174:177], v[170:173]
	s_cmp_ge_u32 s24, 4
	s_cbranch_scc1 .Lskipx111
	s_cmp_eq_u32 s17, 14
	s_cbranch_scc1 .Lskipx111
	global_load_dwordx4 v[186:189], v214, s[12:13]
.Lskipx111:
	s_waitcnt lgkmcnt(1)
	ds_read_b128 v[174:177], v211 offset:15392
	v_mfma_f32_16x16x32_f16 v[158:161], v[66:69], v[178:181], v[158:161]
	v_mfma_f32_16x16x32_f16 v[162:165], v[70:73], v[178:181], v[162:165]
	v_mfma_f32_16x16x32_f16 v[166:169], v[74:77], v[178:181], v[166:169]
	v_mfma_f32_16x16x32_f16 v[170:173], v[78:81], v[178:181], v[170:173]
	global_load_dwordx4 v[190:193], v215, s[8:9]
	s_waitcnt lgkmcnt(1)
	ds_read_b128 v[178:181], v211 offset:15408
	v_mfma_f32_16x16x32_f16 v[158:161], v[82:85], v[182:185], v[158:161]
	v_mfma_f32_16x16x32_f16 v[162:165], v[86:89], v[182:185], v[162:165]
	v_mfma_f32_16x16x32_f16 v[166:169], v[90:93], v[182:185], v[166:169]
	v_mfma_f32_16x16x32_f16 v[170:173], v[94:97], v[182:185], v[170:173]
	s_add_u32 s12, s12, 0x271000
	s_waitcnt lgkmcnt(1)
	ds_read_b128 v[182:185], v210 offset:16640
	v_mfma_f32_16x16x32_f16 v[158:161], v[98:101], v[174:177], v[158:161]
	v_mfma_f32_16x16x32_f16 v[162:165], v[102:105], v[174:177], v[162:165]
	v_mfma_f32_16x16x32_f16 v[166:169], v[106:109], v[174:177], v[166:169]
	v_mfma_f32_16x16x32_f16 v[170:173], v[110:113], v[174:177], v[170:173]
	s_addc_u32 s13, s13, 0
	s_waitcnt lgkmcnt(1)
	ds_read_b128 v[174:177], v210 offset:16656
	v_mfma_f32_16x16x32_f16 v[158:161], v[114:117], v[178:181], v[158:161]
	v_mfma_f32_16x16x32_f16 v[162:165], v[118:121], v[178:181], v[162:165]
	s_add_u32 s8, s8, 0x271000
	v_mfma_f32_16x16x32_f16 v[166:169], v[122:125], v[178:181], v[166:169]
	v_mfma_f32_16x16x32_f16 v[170:173], v[126:129], v[178:181], v[170:173]
	s_addc_u32 s9, s9, 0
	s_waitcnt lgkmcnt(1)
	ds_read_b128 v[178:181], v211 offset:16640
	v_mfma_f32_16x16x32_f16 v[142:145], v[2:5], v[182:185], v[194:197]
	v_mfma_f32_16x16x32_f16 v[146:149], v[6:9], v[182:185], v[198:201]
	v_mfma_f32_16x16x32_f16 v[150:153], v[10:13], v[182:185], v[202:205]
	v_mfma_f32_16x16x32_f16 v[154:157], v[14:17], v[182:185], v[206:209]
	s_waitcnt lgkmcnt(1)
	ds_read_b128 v[182:185], v211 offset:16656
	v_mfma_f32_16x16x32_f16 v[142:145], v[18:21], v[174:177], v[142:145]
	v_mfma_f32_16x16x32_f16 v[146:149], v[22:25], v[174:177], v[146:149]
	v_mfma_f32_16x16x32_f16 v[150:153], v[26:29], v[174:177], v[150:153]
	v_mfma_f32_16x16x32_f16 v[154:157], v[30:33], v[174:177], v[154:157]
	v_exp_f32_e32 v158, v158
	v_exp_f32_e32 v159, v159
	v_exp_f32_e32 v160, v160
	v_exp_f32_e32 v161, v161
	v_exp_f32_e32 v162, v162
	v_exp_f32_e32 v163, v163
	v_exp_f32_e32 v164, v164
	v_exp_f32_e32 v165, v165
	v_exp_f32_e32 v166, v166
	v_exp_f32_e32 v167, v167
	v_exp_f32_e32 v168, v168
	v_exp_f32_e32 v169, v169
	v_exp_f32_e32 v170, v170
	v_exp_f32_e32 v171, v171
	v_exp_f32_e32 v172, v172
	v_exp_f32_e32 v173, v173
	v_add_f32_e32 v166, 1.0, v166
	v_add_f32_e32 v167, 1.0, v167
	v_add_f32_e32 v168, 1.0, v168
	v_add_f32_e32 v169, 1.0, v169
	v_add_f32_e32 v162, 1.0, v162
	v_add_f32_e32 v163, 1.0, v163
	v_add_f32_e32 v164, 1.0, v164
	v_add_f32_e32 v165, 1.0, v165
	v_fma_f32 v158, v158, v166, v166
	v_fma_f32 v159, v159, v167, v167
	v_fma_f32 v160, v160, v168, v168
	v_fma_f32 v161, v161, v169, v169
	v_rcp_f32_e32 v162, v162
	v_rcp_f32_e32 v163, v163
	v_rcp_f32_e32 v164, v164
	v_rcp_f32_e32 v165, v165
	v_fma_f32 v166, v166, v220, s16
	v_fma_f32 v167, v167, v220, s16
	v_fma_f32 v168, v168, v220, s16
	v_fma_f32 v169, v169, v220, s16
	v_rcp_f32_e32 v158, v158
	v_rcp_f32_e32 v159, v159
	v_rcp_f32_e32 v160, v160
	v_rcp_f32_e32 v161, v161
	v_mul_f32_e32 v130, v130, v162
	v_mul_f32_e32 v131, v131, v163
	v_mul_f32_e32 v132, v132, v164
	v_mul_f32_e32 v133, v133, v165
	v_fma_f32 v130, v166, v158, v130
	v_fma_f32 v131, v167, v159, v131
	v_fma_f32 v132, v168, v160, v132
	v_fma_f32 v133, v169, v161, v133
	v_exp_f32_e32 v162, v130
	v_exp_f32_e32 v163, v131
	v_exp_f32_e32 v164, v132
	v_exp_f32_e32 v165, v133
	v_add_f32_e32 v158, 1.0, v162
	v_add_f32_e32 v159, 1.0, v163
	v_add_f32_e32 v160, 1.0, v164
	v_add_f32_e32 v161, 1.0, v165
	v_add_f32_e32 v166, -1.0, v162
	v_add_f32_e32 v167, -1.0, v163
	v_add_f32_e32 v168, -1.0, v164
	v_add_f32_e32 v169, -1.0, v165
	v_fma_f32 v170, v170, v158, v158
	v_fma_f32 v171, v171, v159, v159
	v_fma_f32 v172, v172, v160, v160
	v_fma_f32 v173, v173, v161, v161
	v_rcp_f32_e32 v170, v170
	v_rcp_f32_e32 v171, v171
	v_rcp_f32_e32 v172, v172
	v_rcp_f32_e32 v173, v173
	v_mul_f32_e32 v170, v166, v170
	v_mul_f32_e32 v171, v167, v171
	v_mul_f32_e32 v172, v168, v172
	v_mul_f32_e32 v173, v169, v173
	v_cvt_pk_f16_f32 v170, v170, v171
	v_cvt_pk_f16_f32 v171, v172, v173
	ds_write_b64 v212, v[170:171] offset:0
	s_waitcnt lgkmcnt(2)
	ds_read_b128 v[174:177], v210 offset:16672
	v_mfma_f32_16x16x32_f16 v[142:145], v[66:69], v[178:181], v[142:145]
	v_mfma_f32_16x16x32_f16 v[146:149], v[70:73], v[178:181], v[146:149]
	v_mfma_f32_16x16x32_f16 v[150:153], v[74:77], v[178:181], v[150:153]
	v_mfma_f32_16x16x32_f16 v[154:157], v[78:81], v[178:181], v[154:157]
	s_waitcnt lgkmcnt(2)
	ds_read_b128 v[178:181], v210 offset:16688
	v_mfma_f32_16x16x32_f16 v[142:145], v[82:85], v[182:185], v[142:145]
	v_mfma_f32_16x16x32_f16 v[146:149], v[86:89], v[182:185], v[146:149]
	v_mfma_f32_16x16x32_f16 v[150:153], v[90:93], v[182:185], v[150:153]
	v_mfma_f32_16x16x32_f16 v[154:157], v[94:97], v[182:185], v[154:157]
	s_waitcnt lgkmcnt(1)
	ds_read_b128 v[182:185], v211 offset:16672
	v_mfma_f32_16x16x32_f16 v[142:145], v[34:37], v[174:177], v[142:145]
	v_mfma_f32_16x16x32_f16 v[146:149], v[38:41], v[174:177], v[146:149]
	v_mfma_f32_16x16x32_f16 v[150:153], v[42:45], v[174:177], v[150:153]
	v_mfma_f32_16x16x32_f16 v[154:157], v[46:49], v[174:177], v[154:157]
	s_waitcnt lgkmcnt(1)
	ds_read_b128 v[174:177], v211 offset:16688
	v_mfma_f32_16x16x32_f16 v[142:145], v[50:53], v[178:181], v[142:145]
	v_mfma_f32_16x16x32_f16 v[146:149], v[54:57], v[178:181], v[146:149]
	v_mfma_f32_16x16x32_f16 v[150:153], v[58:61], v[178:181], v[150:153]
	v_mfma_f32_16x16x32_f16 v[154:157], v[62:65], v[178:181], v[154:157]
	s_waitcnt vmcnt(0)
	s_cmp_ge_u32 s24, 4
	s_cbranch_scc1 .Lskips112
	ds_write_b128 v217, v[186:189] offset:15360
.Lskips112:
	ds_write_b128 v217, v[190:193] offset:1280
	s_waitcnt lgkmcnt(3)
	ds_read_b128 v[178:181], v210 offset:17920
	v_mfma_f32_16x16x32_f16 v[142:145], v[98:101], v[182:185], v[142:145]
	v_mfma_f32_16x16x32_f16 v[146:149], v[102:105], v[182:185], v[146:149]
	v_mfma_f32_16x16x32_f16 v[150:153], v[106:109], v[182:185], v[150:153]
	v_mfma_f32_16x16x32_f16 v[154:157], v[110:113], v[182:185], v[154:157]
	s_waitcnt lgkmcnt(3)
	ds_read_b128 v[182:185], v210 offset:17936
	v_mfma_f32_16x16x32_f16 v[142:145], v[114:117], v[174:177], v[142:145]
	v_mfma_f32_16x16x32_f16 v[146:149], v[118:121], v[174:177], v[146:149]
	v_mfma_f32_16x16x32_f16 v[150:153], v[122:125], v[174:177], v[150:153]
	v_mfma_f32_16x16x32_f16 v[154:157], v[126:129], v[174:177], v[154:157]
	s_waitcnt lgkmcnt(1)
	ds_read_b128 v[174:177], v211 offset:17920
	v_mfma_f32_16x16x32_f16 v[158:161], v[2:5], v[178:181], v[194:197]
	v_mfma_f32_16x16x32_f16 v[162:165], v[6:9], v[178:181], v[198:201]
	v_mfma_f32_16x16x32_f16 v[166:169], v[10:13], v[178:181], v[202:205]
	v_mfma_f32_16x16x32_f16 v[170:173], v[14:17], v[178:181], v[206:209]
	s_waitcnt lgkmcnt(1)
	ds_read_b128 v[178:181], v211 offset:17936
	v_mfma_f32_16x16x32_f16 v[158:161], v[18:21], v[182:185], v[158:161]
	v_mfma_f32_16x16x32_f16 v[162:165], v[22:25], v[182:185], v[162:165]
	v_mfma_f32_16x16x32_f16 v[166:169], v[26:29], v[182:185], v[166:169]
	v_mfma_f32_16x16x32_f16 v[170:173], v[30:33], v[182:185], v[170:173]
	v_exp_f32_e32 v142, v142
	v_exp_f32_e32 v143, v143
	v_exp_f32_e32 v144, v144
	v_exp_f32_e32 v145, v145
	v_exp_f32_e32 v146, v146
	v_exp_f32_e32 v147, v147
	v_exp_f32_e32 v148, v148
	v_exp_f32_e32 v149, v149
	v_exp_f32_e32 v150, v150
	v_exp_f32_e32 v151, v151
	v_exp_f32_e32 v152, v152
	v_exp_f32_e32 v153, v153
	v_exp_f32_e32 v154, v154
	v_exp_f32_e32 v155, v155
	v_exp_f32_e32 v156, v156
	v_exp_f32_e32 v157, v157
	v_add_f32_e32 v150, 1.0, v150
	v_add_f32_e32 v151, 1.0, v151
	v_add_f32_e32 v152, 1.0, v152
	v_add_f32_e32 v153, 1.0, v153
	v_add_f32_e32 v146, 1.0, v146
	v_add_f32_e32 v147, 1.0, v147
	v_add_f32_e32 v148, 1.0, v148
	v_add_f32_e32 v149, 1.0, v149
	v_fma_f32 v142, v142, v150, v150
	v_fma_f32 v143, v143, v151, v151
	v_fma_f32 v144, v144, v152, v152
	v_fma_f32 v145, v145, v153, v153
	v_rcp_f32_e32 v146, v146
	v_rcp_f32_e32 v147, v147
	v_rcp_f32_e32 v148, v148
	v_rcp_f32_e32 v149, v149
	v_fma_f32 v150, v150, v220, s16
	v_fma_f32 v151, v151, v220, s16
	v_fma_f32 v152, v152, v220, s16
	v_fma_f32 v153, v153, v220, s16
	v_rcp_f32_e32 v142, v142
	v_rcp_f32_e32 v143, v143
	v_rcp_f32_e32 v144, v144
	v_rcp_f32_e32 v145, v145
	v_mul_f32_e32 v134, v134, v146
	v_mul_f32_e32 v135, v135, v147
	v_mul_f32_e32 v136, v136, v148
	v_mul_f32_e32 v137, v137, v149
	v_fma_f32 v134, v150, v142, v134
	v_fma_f32 v135, v151, v143, v135
	v_fma_f32 v136, v152, v144, v136
	v_fma_f32 v137, v153, v145, v137
	v_exp_f32_e32 v146, v134
	v_exp_f32_e32 v147, v135
	v_exp_f32_e32 v148, v136
	v_exp_f32_e32 v149, v137
	v_add_f32_e32 v142, 1.0, v146
	v_add_f32_e32 v143, 1.0, v147
	v_add_f32_e32 v144, 1.0, v148
	v_add_f32_e32 v145, 1.0, v149
	v_add_f32_e32 v150, -1.0, v146
	v_add_f32_e32 v151, -1.0, v147
	v_add_f32_e32 v152, -1.0, v148
	v_add_f32_e32 v153, -1.0, v149
	v_fma_f32 v154, v154, v142, v142
	v_fma_f32 v155, v155, v143, v143
	v_fma_f32 v156, v156, v144, v144
	v_fma_f32 v157, v157, v145, v145
	v_rcp_f32_e32 v154, v154
	v_rcp_f32_e32 v155, v155
	v_rcp_f32_e32 v156, v156
	v_rcp_f32_e32 v157, v157
	v_mul_f32_e32 v154, v150, v154
	v_mul_f32_e32 v155, v151, v155
	v_mul_f32_e32 v156, v152, v156
	v_mul_f32_e32 v157, v153, v157
	v_cvt_pk_f16_f32 v154, v154, v155
	v_cvt_pk_f16_f32 v155, v156, v157
	ds_write_b64 v212, v[154:155] offset:1280
	s_waitcnt lgkmcnt(2)
	ds_read_b128 v[182:185], v210 offset:17952
	v_mfma_f32_16x16x32_f16 v[158:161], v[66:69], v[174:177], v[158:161]
	v_mfma_f32_16x16x32_f16 v[162:165], v[70:73], v[174:177], v[162:165]
	v_mfma_f32_16x16x32_f16 v[166:169], v[74:77], v[174:177], v[166:169]
	v_mfma_f32_16x16x32_f16 v[170:173], v[78:81], v[174:177], v[170:173]
	s_waitcnt lgkmcnt(2)
	ds_read_b128 v[174:177], v210 offset:17968
	v_mfma_f32_16x16x32_f16 v[158:161], v[82:85], v[178:181], v[158:161]
	v_mfma_f32_16x16x32_f16 v[162:165], v[86:89], v[178:181], v[162:165]
	v_mfma_f32_16x16x32_f16 v[166:169], v[90:93], v[178:181], v[166:169]
	v_mfma_f32_16x16x32_f16 v[170:173], v[94:97], v[178:181], v[170:173]
	s_waitcnt lgkmcnt(1)
	ds_read_b128 v[178:181], v211 offset:17952
	v_mfma_f32_16x16x32_f16 v[158:161], v[34:37], v[182:185], v[158:161]
	v_mfma_f32_16x16x32_f16 v[162:165], v[38:41], v[182:185], v[162:165]
	v_mfma_f32_16x16x32_f16 v[166:169], v[42:45], v[182:185], v[166:169]
	v_mfma_f32_16x16x32_f16 v[170:173], v[46:49], v[182:185], v[170:173]
	s_waitcnt lgkmcnt(1)
	ds_read_b128 v[182:185], v211 offset:17968
	v_mfma_f32_16x16x32_f16 v[158:161], v[50:53], v[174:177], v[158:161]
	v_mfma_f32_16x16x32_f16 v[162:165], v[54:57], v[174:177], v[162:165]
	v_mfma_f32_16x16x32_f16 v[166:169], v[58:61], v[174:177], v[166:169]
	v_mfma_f32_16x16x32_f16 v[170:173], v[62:65], v[174:177], v[170:173]
	s_waitcnt lgkmcnt(1)
	ds_read_b128 v[174:177], v210 offset:0
	v_mfma_f32_16x16x32_f16 v[158:161], v[98:101], v[178:181], v[158:161]
	v_mfma_f32_16x16x32_f16 v[162:165], v[102:105], v[178:181], v[162:165]
	v_mfma_f32_16x16x32_f16 v[166:169], v[106:109], v[178:181], v[166:169]
	v_mfma_f32_16x16x32_f16 v[170:173], v[110:113], v[178:181], v[170:173]
	s_waitcnt lgkmcnt(1)
	ds_read_b128 v[178:181], v210 offset:16
	v_mfma_f32_16x16x32_f16 v[158:161], v[114:117], v[182:185], v[158:161]
	v_mfma_f32_16x16x32_f16 v[162:165], v[118:121], v[182:185], v[162:165]
	v_mfma_f32_16x16x32_f16 v[166:169], v[122:125], v[182:185], v[166:169]
	v_mfma_f32_16x16x32_f16 v[170:173], v[126:129], v[182:185], v[170:173]
	s_waitcnt lgkmcnt(1)
	ds_read_b128 v[182:185], v210 offset:32
	v_mfma_f32_16x16x32_f16 v[142:145], v[2:5], v[174:177], v[194:197]
	v_mfma_f32_16x16x32_f16 v[146:149], v[6:9], v[174:177], v[198:201]
	v_mfma_f32_16x16x32_f16 v[150:153], v[10:13], v[174:177], v[202:205]
	v_mfma_f32_16x16x32_f16 v[154:157], v[14:17], v[174:177], v[206:209]
	s_waitcnt lgkmcnt(1)
	ds_read_b128 v[174:177], v210 offset:48
	v_mfma_f32_16x16x32_f16 v[142:145], v[18:21], v[178:181], v[142:145]
	v_mfma_f32_16x16x32_f16 v[146:149], v[22:25], v[178:181], v[146:149]
	v_mfma_f32_16x16x32_f16 v[150:153], v[26:29], v[178:181], v[150:153]
	v_mfma_f32_16x16x32_f16 v[154:157], v[30:33], v[178:181], v[154:157]
	v_exp_f32_e32 v158, v158
	v_exp_f32_e32 v159, v159
	v_exp_f32_e32 v160, v160
	v_exp_f32_e32 v161, v161
	v_exp_f32_e32 v162, v162
	v_exp_f32_e32 v163, v163
	v_exp_f32_e32 v164, v164
	v_exp_f32_e32 v165, v165
	v_exp_f32_e32 v166, v166
	v_exp_f32_e32 v167, v167
	v_exp_f32_e32 v168, v168
	v_exp_f32_e32 v169, v169
	v_exp_f32_e32 v170, v170
	v_exp_f32_e32 v171, v171
	v_exp_f32_e32 v172, v172
	v_exp_f32_e32 v173, v173
	v_add_f32_e32 v166, 1.0, v166
	v_add_f32_e32 v167, 1.0, v167
	v_add_f32_e32 v168, 1.0, v168
	v_add_f32_e32 v169, 1.0, v169
	v_add_f32_e32 v162, 1.0, v162
	v_add_f32_e32 v163, 1.0, v163
	v_add_f32_e32 v164, 1.0, v164
	v_add_f32_e32 v165, 1.0, v165
	v_fma_f32 v158, v158, v166, v166
	v_fma_f32 v159, v159, v167, v167
	v_fma_f32 v160, v160, v168, v168
	v_fma_f32 v161, v161, v169, v169
	v_rcp_f32_e32 v162, v162
	v_rcp_f32_e32 v163, v163
	v_rcp_f32_e32 v164, v164
	v_rcp_f32_e32 v165, v165
	v_fma_f32 v166, v166, v220, s16
	v_fma_f32 v167, v167, v220, s16
	v_fma_f32 v168, v168, v220, s16
	v_fma_f32 v169, v169, v220, s16
	v_rcp_f32_e32 v158, v158
	v_rcp_f32_e32 v159, v159
	v_rcp_f32_e32 v160, v160
	v_rcp_f32_e32 v161, v161
	v_mul_f32_e32 v138, v138, v162
	v_mul_f32_e32 v139, v139, v163
	v_mul_f32_e32 v140, v140, v164
	v_mul_f32_e32 v141, v141, v165
	v_fma_f32 v138, v166, v158, v138
	v_fma_f32 v139, v167, v159, v139
	v_fma_f32 v140, v168, v160, v140
	v_fma_f32 v141, v169, v161, v141
	v_exp_f32_e32 v162, v138
	v_exp_f32_e32 v163, v139
	v_exp_f32_e32 v164, v140
	v_exp_f32_e32 v165, v141
	v_add_f32_e32 v158, 1.0, v162
	v_add_f32_e32 v159, 1.0, v163
	v_add_f32_e32 v160, 1.0, v164
	v_add_f32_e32 v161, 1.0, v165
	v_add_f32_e32 v166, -1.0, v162
	v_add_f32_e32 v167, -1.0, v163
	v_add_f32_e32 v168, -1.0, v164
	v_add_f32_e32 v169, -1.0, v165
	v_fma_f32 v170, v170, v158, v158
	v_fma_f32 v171, v171, v159, v159
	v_fma_f32 v172, v172, v160, v160
	v_fma_f32 v173, v173, v161, v161
	v_rcp_f32_e32 v170, v170
	v_rcp_f32_e32 v171, v171
	v_rcp_f32_e32 v172, v172
	v_rcp_f32_e32 v173, v173
	v_mul_f32_e32 v170, v166, v170
	v_mul_f32_e32 v171, v167, v171
	v_mul_f32_e32 v172, v168, v172
	v_mul_f32_e32 v173, v169, v173
	v_cvt_pk_f16_f32 v170, v170, v171
	v_cvt_pk_f16_f32 v171, v172, v173
	ds_write_b64 v212, v[170:171] offset:2560
	s_waitcnt lgkmcnt(0)
	s_barrier
	s_add_u32 s17, s17, 2
	s_cmp_lt_u32 s17, 16
	s_cbranch_scc1 .Llstm2_loop
	s_waitcnt lgkmcnt(0)
	v_bfe_u32 v221, v0, 4, 2
	v_lshrrev_b32_e32 v222, 6, v0
	s_mul_i32 s22, s2, 48
	v_lshl_add_u32 v216, v222, 2, v221
	v_lshlrev_b32_e32 v216, 4, v216
	global_load_dwordx4 v[158:161], v216, s[28:29]
	global_load_dwordx4 v[162:165], v216, s[30:31]
	ds_read_b128 v[174:177], v211 offset:0
	ds_read_b128 v[178:181], v211 offset:1280
	ds_read_b128 v[182:185], v211 offset:2560
	s_waitcnt lgkmcnt(2)
	v_mfma_f32_16x16x32_f16 v[226:229], v[238:241], v[174:177], v[226:229]
	ds_read_b128 v[174:177], v211 offset:16
	s_waitcnt lgkmcnt(2)
	v_mfma_f32_16x16x32_f16 v[230:233], v[238:241], v[178:181], v[230:233]
	ds_read_b128 v[178:181], v211 offset:1296
	s_waitcnt lgkmcnt(2)
	v_mfma_f32_16x16x32_f16 v[234:237], v[238:241], v[182:185], v[234:237]
	ds_read_b128 v[182:185], v211 offset:2576
	s_waitcnt lgkmcnt(2)
	v_mfma_f32_16x16x32_f16 v[226:229], v[242:245], v[174:177], v[226:229]
	ds_read_b128 v[174:177], v211 offset:32
	s_waitcnt lgkmcnt(2)
	v_mfma_f32_16x16x32_f16 v[230:233], v[242:245], v[178:181], v[230:233]
	ds_read_b128 v[178:181], v211 offset:1312
	s_waitcnt lgkmcnt(2)
	v_mfma_f32_16x16x32_f16 v[234:237], v[242:245], v[182:185], v[234:237]
	ds_read_b128 v[182:185], v211 offset:2592
	s_waitcnt lgkmcnt(2)
	v_mfma_f32_16x16x32_f16 v[226:229], v[246:249], v[174:177], v[226:229]
	ds_read_b128 v[174:177], v211 offset:48
	s_waitcnt lgkmcnt(2)
	v_mfma_f32_16x16x32_f16 v[230:233], v[246:249], v[178:181], v[230:233]
	ds_read_b128 v[178:181], v211 offset:1328
	s_waitcnt lgkmcnt(2)
	v_mfma_f32_16x16x32_f16 v[234:237], v[246:249], v[182:185], v[234:237]
	ds_read_b128 v[182:185], v211 offset:2608
	s_waitcnt lgkmcnt(2)
	v_mfma_f32_16x16x32_f16 v[226:229], v[250:253], v[174:177], v[226:229]
	s_waitcnt lgkmcnt(1)
	v_mfma_f32_16x16x32_f16 v[230:233], v[250:253], v[178:181], v[230:233]
	s_waitcnt lgkmcnt(0)
	v_mfma_f32_16x16x32_f16 v[234:237], v[250:253], v[182:185], v[234:237]
	s_waitcnt vmcnt(0)
	s_nop 7
	s_nop 1
	v_add_f32_e32 v226, v226, v158
	v_add_f32_e32 v227, v227, v159
	v_add_f32_e32 v228, v228, v160
	v_add_f32_e32 v229, v229, v161
	v_max_f32_e32 v226, 0, v226
	v_max_f32_e32 v227, 0, v227
	v_max_f32_e32 v228, 0, v228
	v_max_f32_e32 v229, 0, v229
	v_mul_f32_e32 v166, v226, v162
	v_fma_f32 v166, v227, v163, v166
	v_fma_f32 v166, v228, v164, v166
	v_fma_f32 v166, v229, v165, v166
	ds_write_b32 v224, v166 offset:0
	v_add_f32_e32 v230, v230, v158
	v_add_f32_e32 v231, v231, v159
	v_add_f32_e32 v232, v232, v160
	v_add_f32_e32 v233, v233, v161
	v_max_f32_e32 v230, 0, v230
	v_max_f32_e32 v231, 0, v231
	v_max_f32_e32 v232, 0, v232
	v_max_f32_e32 v233, 0, v233
	v_mul_f32_e32 v167, v230, v162
	v_fma_f32 v167, v231, v163, v167
	v_fma_f32 v167, v232, v164, v167
	v_fma_f32 v167, v233, v165, v167
	ds_write_b32 v224, v167 offset:2048
	v_add_f32_e32 v234, v234, v158
	v_add_f32_e32 v235, v235, v159
	v_add_f32_e32 v236, v236, v160
	v_add_f32_e32 v237, v237, v161
	v_max_f32_e32 v234, 0, v234
	v_max_f32_e32 v235, 0, v235
	v_max_f32_e32 v236, 0, v236
	v_max_f32_e32 v237, 0, v237
	v_mul_f32_e32 v168, v234, v162
	v_fma_f32 v168, v235, v163, v168
	v_fma_f32 v168, v236, v164, v168
	v_fma_f32 v168, v237, v165, v168
	ds_write_b32 v224, v168 offset:4096
	s_waitcnt lgkmcnt(0)
	s_barrier
	v_add_u32_e32 v221, s22, v0
	s_movk_i32 s23, 0x2710
	v_cmp_gt_u32_e64 s[16:17], s23, v221
	v_cmp_gt_u32_e64 s[18:19], 48, v0
	s_nop 3
	s_and_b64 s[16:17], s[16:17], s[18:19]
	s_and_saveexec_b64 s[18:19], s[16:17]
	s_cbranch_execz .Ll2_end
	v_lshlrev_b32_e32 v1, 7, v0
	v_add_u32_e32 v1, 0x13400, v1
	ds_read_b128 v[2:5], v1 offset:0
	ds_read_b128 v[6:9], v1 offset:16
	ds_read_b128 v[10:13], v1 offset:32
	ds_read_b128 v[14:17], v1 offset:48
	ds_read_b128 v[18:21], v1 offset:64
	ds_read_b128 v[22:25], v1 offset:80
	ds_read_b128 v[26:29], v1 offset:96
	ds_read_b128 v[30:33], v1 offset:112
	s_load_dword s20, s[32:33], 0x0
	s_waitcnt lgkmcnt(0)
	v_mov_b32_e32 v222, s20
	v_add_f32_e32 v222, v222, v2
	v_add_f32_e32 v222, v222, v3
	v_add_f32_e32 v222, v222, v4
	v_add_f32_e32 v222, v222, v5
	v_add_f32_e32 v222, v222, v6
	v_add_f32_e32 v222, v222, v7
	v_add_f32_e32 v222, v222, v8
	v_add_f32_e32 v222, v222, v9
	v_add_f32_e32 v222, v222, v10
	v_add_f32_e32 v222, v222, v11
	v_add_f32_e32 v222, v222, v12
	v_add_f32_e32 v222, v222, v13
	v_add_f32_e32 v222, v222, v14
	v_add_f32_e32 v222, v222, v15
	v_add_f32_e32 v222, v222, v16
	v_add_f32_e32 v222, v222, v17
	v_add_f32_e32 v222, v222, v18
	v_add_f32_e32 v222, v222, v19
	v_add_f32_e32 v222, v222, v20
	v_add_f32_e32 v222, v222, v21
	v_add_f32_e32 v222, v222, v22
	v_add_f32_e32 v222, v222, v23
	v_add_f32_e32 v222, v222, v24
	v_add_f32_e32 v222, v222, v25
	v_add_f32_e32 v222, v222, v26
	v_add_f32_e32 v222, v222, v27
	v_add_f32_e32 v222, v222, v28
	v_add_f32_e32 v222, v222, v29
	v_add_f32_e32 v222, v222, v30
	v_add_f32_e32 v222, v222, v31
	v_add_f32_e32 v222, v222, v32
	v_add_f32_e32 v222, v222, v33
	v_max_f32_e32 v222, 0, v222
	v_lshlrev_b32_e32 v221, 2, v221
	global_store_dword v221, v222, s[34:35]

	.amdhsa_kernel _Z6k_lstmILi128ELi8ELb0ELb1EEvPKDF16_S1_S1_PKfPDF16_S1_S1_S1_S3_S3_S3_PfS5_
		.amdhsa_group_segment_fixed_size 0
		.amdhsa_private_segment_fixed_size 0
		.amdhsa_kernarg_size 104
		.amdhsa_user_sgpr_count 2
		.amdhsa_user_sgpr_dispatch_ptr 0
		.amdhsa_user_sgpr_queue_ptr 0
		.amdhsa_user_sgpr_kernarg_segment_ptr 1
		.amdhsa_user_sgpr_dispatch_id 0
		.amdhsa_user_sgpr_kernarg_preload_length 0
		.amdhsa_user_sgpr_kernarg_preload_offset 0
		.amdhsa_user_sgpr_private_segment_size 0
		.amdhsa_uses_dynamic_stack 0
		.amdhsa_enable_private_segment 0
		.amdhsa_system_sgpr_workgroup_id_x 1
		.amdhsa_system_sgpr_workgroup_id_y 0
		.amdhsa_system_sgpr_workgroup_id_z 0
		.amdhsa_system_sgpr_workgroup_info 0
		.amdhsa_system_vgpr_workitem_id 0
		.amdhsa_next_free_vgpr 256
		.amdhsa_next_free_sgpr 40
		.amdhsa_accum_offset 256
		.amdhsa_reserve_vcc 1
		.amdhsa_float_round_mode_32 0
		.amdhsa_float_round_mode_16_64 0
		.amdhsa_float_denorm_mode_32 3
		.amdhsa_float_denorm_mode_16_64 3
		.amdhsa_dx10_clamp 1
		.amdhsa_ieee_mode 1
		.amdhsa_fp16_overflow 0
		.amdhsa_tg_split 0
		.amdhsa_exception_fp_ieee_invalid_op 0
		.amdhsa_exception_fp_denorm_src 0
		.amdhsa_exception_fp_ieee_div_zero 0
		.amdhsa_exception_fp_ieee_overflow 0
		.amdhsa_exception_fp_ieee_underflow 0
		.amdhsa_exception_fp_ieee_inexact 0
		.amdhsa_exception_int_div_zero 0
	.end_amdhsa_kernel

amdhsa.kernels:
  - .agpr_count:     0
    .args:
      - .actual_access:  read_only
        .address_space:  global
        .offset:         0
        .size:           8
        .value_kind:     global_buffer
      - .actual_access:  read_only
        .address_space:  global
        .offset:         8
        .size:           8
        .value_kind:     global_buffer
      - .actual_access:  read_only
        .address_space:  global
        .offset:         16
        .size:           8
        .value_kind:     global_buffer
      - .actual_access:  read_only
        .address_space:  global
        .offset:         24
        .size:           8
        .value_kind:     global_buffer
      - .actual_access:  write_only
        .address_space:  global
        .offset:         32
        .size:           8
        .value_kind:     global_buffer
      - .actual_access:  write_only
        .address_space:  global
        .offset:         40
        .size:           8
        .value_kind:     global_buffer
    .group_segment_fixed_size: 56512
    .kernarg_segment_align: 8
    .kernarg_segment_size: 48
    .language:       OpenCL C
    .language_version:
      - 2
      - 0
    .max_flat_workgroup_size: 1024
    .name:           _Z10k_bscatterPKiS0_PKfS0_PiP15HIP_vector_typeIiLj2EE
    .private_segment_fixed_size: 0
    .sgpr_count:     42
    .sgpr_spill_count: 0
    .symbol:         _Z10k_bscatterPKiS0_PKfS0_PiP15HIP_vector_typeIiLj2EE.kd
    .uniform_work_group_size: 1
    .uses_dynamic_stack: false
    .vgpr_count:     89
    .vgpr_spill_count: 0
    .wavefront_size: 64
  - .agpr_count:     0
    .args:
      - .actual_access:  read_only
        .address_space:  global
        .offset:         0
        .size:           8
        .value_kind:     global_buffer
      - .actual_access:  read_only
        .address_space:  global
        .offset:         8
        .size:           8
        .value_kind:     global_buffer
      - .actual_access:  write_only
        .address_space:  global
        .offset:         16
        .size:           8
        .value_kind:     global_buffer
      - .actual_access:  write_only
        .address_space:  global
        .offset:         24
        .size:           8
        .value_kind:     global_buffer
      - .actual_access:  write_only
        .address_space:  global
        .offset:         32
        .size:           8
        .value_kind:     global_buffer
      - .actual_access:  write_only
        .address_space:  global
        .offset:         40
        .size:           8
        .value_kind:     global_buffer
      - .actual_access:  read_only
        .address_space:  global
        .offset:         48
        .size:           8
        .value_kind:     global_buffer
      - .actual_access:  write_only
        .address_space:  global
        .offset:         56
        .size:           8
        .value_kind:     global_buffer
    .group_segment_fixed_size: 12352
    .kernarg_segment_align: 8
    .kernarg_segment_size: 64
    .language:       OpenCL C
    .language_version:
      - 2
      - 0
    .max_flat_workgroup_size: 1024
    .name:           _Z8k_bfinalPK15HIP_vector_typeIiLj2EEPKiPS0_PiS6_PfPKfPDF16_
    .private_segment_fixed_size: 0
    .sgpr_count:     38
    .sgpr_spill_count: 0
    .symbol:         _Z8k_bfinalPK15HIP_vector_typeIiLj2EEPKiPS0_PiS6_PfPKfPDF16_.kd
    .uniform_work_group_size: 1
    .uses_dynamic_stack: false
    .vgpr_count:     72
    .vgpr_spill_count: 0
    .wavefront_size: 64
  - .agpr_count:     0
    .args:
      - .actual_access:  read_only
        .address_space:  global
        .offset:         0
        .size:           8
        .value_kind:     global_buffer
      - .actual_access:  write_only
        .address_space:  global
        .offset:         8
        .size:           8
        .value_kind:     global_buffer
      - .actual_access:  write_only
        .address_space:  global
        .offset:         16
        .size:           8
        .value_kind:     global_buffer
      - .actual_access:  read_only
        .address_space:  global
        .offset:         24
        .size:           8
        .value_kind:     global_buffer
      - .actual_access:  read_only
        .address_space:  global
        .offset:         32
        .size:           8
        .value_kind:     global_buffer
      - .actual_access:  write_only
        .address_space:  global
        .offset:         40
        .size:           8
        .value_kind:     global_buffer
      - .actual_access:  read_only
        .address_space:  global
        .offset:         48
        .size:           8
        .value_kind:     global_buffer
      - .actual_access:  read_only
        .address_space:  global
        .offset:         56
        .size:           8
        .value_kind:     global_buffer
      - .actual_access:  read_only
        .address_space:  global
        .offset:         64
        .size:           8
        .value_kind:     global_buffer
      - .actual_access:  read_only
        .address_space:  global
        .offset:         72
        .size:           8
        .value_kind:     global_buffer
      - .actual_access:  read_only
        .address_space:  global
        .offset:         80
        .size:           8
        .value_kind:     global_buffer
      - .actual_access:  read_only
        .address_space:  global
        .offset:         88
        .size:           8
        .value_kind:     global_buffer
      - .actual_access:  write_only
        .address_space:  global
        .offset:         96
        .size:           8
        .value_kind:     global_buffer
      - .actual_access:  write_only
        .address_space:  global
        .offset:         104
        .size:           8
        .value_kind:     global_buffer
      - .actual_access:  write_only
        .address_space:  global
        .offset:         112
        .size:           8
        .value_kind:     global_buffer
      - .actual_access:  write_only
        .address_space:  global
        .offset:         120
        .size:           8
        .value_kind:     global_buffer
      - .actual_access:  write_only
        .address_space:  global
        .offset:         128
        .size:           8
        .value_kind:     global_buffer
    .group_segment_fixed_size: 628
    .kernarg_segment_align: 8
    .kernarg_segment_size: 136
    .language:       OpenCL C
    .language_version:
      - 2
      - 0
    .max_flat_workgroup_size: 1024
    .name:           _Z7k_bhistPKiPiPfPKfS4_PDF16_S4_S4_S4_S4_S4_S4_S5_S5_S5_S5_S2_
    .private_segment_fixed_size: 0
    .sgpr_count:     25
    .sgpr_spill_count: 0
    .symbol:         _Z7k_bhistPKiPiPfPKfS4_PDF16_S4_S4_S4_S4_S4_S4_S5_S5_S5_S5_S2_.kd
    .uniform_work_group_size: 1
    .uses_dynamic_stack: false
    .vgpr_count:     32
    .vgpr_spill_count: 0
    .wavefront_size: 64
  - .agpr_count:     0
    .args:
      - .actual_access:  read_only
        .address_space:  global
        .offset:         0
        .size:           8
        .value_kind:     global_buffer
      - .actual_access:  read_only
        .address_space:  global
        .offset:         8
        .size:           8
        .value_kind:     global_buffer
      - .actual_access:  read_only
        .address_space:  global
        .offset:         16
        .size:           8
        .value_kind:     global_buffer
      - .actual_access:  read_only
        .address_space:  global
        .offset:         24
        .size:           8
        .value_kind:     global_buffer
      - .actual_access:  read_only
        .address_space:  global
        .offset:         32
        .size:           8
        .value_kind:     global_buffer
      - .actual_access:  read_only
        .address_space:  global
        .offset:         40
        .size:           8
        .value_kind:     global_buffer
      - .actual_access:  read_only
        .address_space:  global
        .offset:         48
        .size:           8
        .value_kind:     global_buffer
      - .actual_access:  read_only
        .address_space:  global
        .offset:         56
        .size:           8
        .value_kind:     global_buffer
      - .actual_access:  read_only
        .address_space:  global
        .offset:         64
        .size:           8
        .value_kind:     global_buffer
      - .actual_access:  write_only
        .address_space:  global
        .offset:         72
        .size:           8
        .value_kind:     global_buffer
      - .actual_access:  write_only
        .address_space:  global
        .offset:         80
        .size:           8
        .value_kind:     global_buffer
      - .offset:         88
        .size:           4
        .value_kind:     hidden_block_count_x
      - .offset:         92
        .size:           4
        .value_kind:     hidden_block_count_y
      - .offset:         96
        .size:           4
        .value_kind:     hidden_block_count_z
      - .offset:         100
        .size:           2
        .value_kind:     hidden_group_size_x
      - .offset:         102
        .size:           2
        .value_kind:     hidden_group_size_y
      - .offset:         104
        .size:           2
        .value_kind:     hidden_group_size_z
      - .offset:         106
        .size:           2
        .value_kind:     hidden_remainder_x
      - .offset:         108
        .size:           2
        .value_kind:     hidden_remainder_y
      - .offset:         110
        .size:           2
        .value_kind:     hidden_remainder_z
      - .offset:         128
        .size:           8
        .value_kind:     hidden_global_offset_x
      - .offset:         136
        .size:           8
        .value_kind:     hidden_global_offset_y
      - .offset:         144
        .size:           8
        .value_kind:     hidden_global_offset_z
      - .offset:         152
        .size:           2
        .value_kind:     hidden_grid_dims
    .group_segment_fixed_size: 2048
    .kernarg_segment_align: 8
    .kernarg_segment_size: 344
    .language:       OpenCL C
    .language_version:
      - 2
      - 0
    .max_flat_workgroup_size: 256
    .name:           _Z7k_fold2PKfS0_S0_S0_S0_S0_S0_S0_S0_PDF16_Pf
    .private_segment_fixed_size: 0
    .sgpr_count:     36
    .sgpr_spill_count: 0
    .symbol:         _Z7k_fold2PKfS0_S0_S0_S0_S0_S0_S0_S0_PDF16_Pf.kd
    .uniform_work_group_size: 1
    .uses_dynamic_stack: false
    .vgpr_count:     61
    .vgpr_spill_count: 0
    .wavefront_size: 64
  - .agpr_count:     0
    .args:
      - .actual_access:  read_only
        .address_space:  global
        .offset:         0
        .size:           8
        .value_kind:     global_buffer
      - .actual_access:  read_only
        .address_space:  global
        .offset:         8
        .size:           8
        .value_kind:     global_buffer
      - .actual_access:  write_only
        .address_space:  global
        .offset:         16
        .size:           8
        .value_kind:     global_buffer
      - .actual_access:  read_only
        .address_space:  global
        .offset:         24
        .size:           8
        .value_kind:     global_buffer
      - .actual_access:  read_only
        .address_space:  global
        .offset:         32
        .size:           8
        .value_kind:     global_buffer
      - .actual_access:  read_only
        .address_space:  global
        .offset:         40
        .size:           8
        .value_kind:     global_buffer
      - .actual_access:  read_only
        .address_space:  global
        .offset:         48
        .size:           8
        .value_kind:     global_buffer
      - .actual_access:  read_only
        .address_space:  global
        .offset:         56
        .size:           8
        .value_kind:     global_buffer
      - .actual_access:  read_only
        .address_space:  global
        .offset:         64
        .size:           8
        .value_kind:     global_buffer
      - .actual_access:  read_only
        .address_space:  global
        .offset:         72
        .size:           8
        .value_kind:     global_buffer
      - .actual_access:  read_only
        .address_space:  global
        .offset:         80
        .size:           8
        .value_kind:     global_buffer
      - .actual_access:  write_only
        .address_space:  global
        .offset:         88
        .size:           8
        .value_kind:     global_buffer
      - .actual_access:  write_only
        .address_space:  global
        .offset:         96
        .size:           8
        .value_kind:     global_buffer
      - .address_space:  global
        .offset:         104
        .size:           8
        .value_kind:     global_buffer
      - .actual_access:  write_only
        .address_space:  global
        .offset:         112
        .size:           8
        .value_kind:     global_buffer
      - .actual_access:  read_only
        .address_space:  global
        .offset:         120
        .size:           8
        .value_kind:     global_buffer
      - .actual_access:  read_only
        .address_space:  global
        .offset:         128
        .size:           8
        .value_kind:     global_buffer
    .group_segment_fixed_size: 22272
    .kernarg_segment_align: 8
    .kernarg_segment_size: 136
    .language:       OpenCL C
    .language_version:
      - 2
      - 0
    .max_flat_workgroup_size: 256
    .name:           _Z5k_gcnILi1EEvPKvPK15HIP_vector_typeIiLj2EEPfPKiS8_PKfPKDF16_SA_SA_SA_SA_S6_PDF16_S6_SD_SC_SA_
    .private_segment_fixed_size: 0
    .sgpr_count:     35
    .sgpr_spill_count: 0
    .symbol:         _Z5k_gcnILi1EEvPKvPK15HIP_vector_typeIiLj2EEPfPKiS8_PKfPKDF16_SA_SA_SA_SA_S6_PDF16_S6_SD_SC_SA_.kd
    .uniform_work_group_size: 1
    .uses_dynamic_stack: false
    .vgpr_count:     58
    .vgpr_spill_count: 0
    .wavefront_size: 64
  - .agpr_count:     0
    .args:
      - .actual_access:  read_only
        .address_space:  global
        .offset:         0
        .size:           8
        .value_kind:     global_buffer
      - .actual_access:  read_only
        .address_space:  global
        .offset:         8
        .size:           8
        .value_kind:     global_buffer
      - .actual_access:  read_only
        .address_space:  global
        .offset:         16
        .size:           8
        .value_kind:     global_buffer
      - .actual_access:  read_only
        .address_space:  global
        .offset:         24
        .size:           8
        .value_kind:     global_buffer
      - .actual_access:  read_only
        .address_space:  global
        .offset:         32
        .size:           8
        .value_kind:     global_buffer
      - .actual_access:  read_only
        .address_space:  global
        .offset:         40
        .size:           8
        .value_kind:     global_buffer
      - .actual_access:  read_only
        .address_space:  global
        .offset:         48
        .size:           8
        .value_kind:     global_buffer
      - .actual_access:  read_only
        .address_space:  global
        .offset:         56
        .size:           8
        .value_kind:     global_buffer
      - .actual_access:  read_only
        .address_space:  global
        .offset:         64
        .size:           8
        .value_kind:     global_buffer
      - .actual_access:  read_only
        .address_space:  global
        .offset:         72
        .size:           8
        .value_kind:     global_buffer
      - .actual_access:  read_only
        .address_space:  global
        .offset:         80
        .size:           8
        .value_kind:     global_buffer
      - .actual_access:  read_only
        .address_space:  global
        .offset:         88
        .size:           8
        .value_kind:     global_buffer
      - .actual_access:  write_only
        .address_space:  global
        .offset:         96
        .size:           8
        .value_kind:     global_buffer
      - .address_space:  global
        .offset:         104
        .size:           8
        .value_kind:     global_buffer
      - .actual_access:  read_only
        .address_space:  global
        .offset:         112
        .size:           8
        .value_kind:     global_buffer
      - .actual_access:  read_only
        .address_space:  global
        .offset:         120
        .size:           8
        .value_kind:     global_buffer
      - .actual_access:  read_only
        .address_space:  global
        .offset:         128
        .size:           8
        .value_kind:     global_buffer
      - .offset:         136
        .size:           4
        .value_kind:     hidden_block_count_x
      - .offset:         140
        .size:           4
        .value_kind:     hidden_block_count_y
      - .offset:         144
        .size:           4
        .value_kind:     hidden_block_count_z
      - .offset:         148
        .size:           2
        .value_kind:     hidden_group_size_x
      - .offset:         150
        .size:           2
        .value_kind:     hidden_group_size_y
      - .offset:         152
        .size:           2
        .value_kind:     hidden_group_size_z
      - .offset:         154
        .size:           2
        .value_kind:     hidden_remainder_x
      - .offset:         156
        .size:           2
        .value_kind:     hidden_remainder_y
      - .offset:         158
        .size:           2
        .value_kind:     hidden_remainder_z
      - .offset:         176
        .size:           8
        .value_kind:     hidden_global_offset_x
      - .offset:         184
        .size:           8
        .value_kind:     hidden_global_offset_y
      - .offset:         192
        .size:           8
        .value_kind:     hidden_global_offset_z
      - .offset:         200
        .size:           2
        .value_kind:     hidden_grid_dims
    .group_segment_fixed_size: 23808
    .kernarg_segment_align: 8
    .kernarg_segment_size: 392
    .language:       OpenCL C
    .language_version:
      - 2
      - 0
    .max_flat_workgroup_size: 256
    .name:           _Z5k_gcnILi2EEvPKvPK15HIP_vector_typeIiLj2EEPfPKiS8_PKfPKDF16_SA_SA_SA_SA_S6_PDF16_S6_SD_SC_SA_
    .private_segment_fixed_size: 0
    .sgpr_count:     36
    .sgpr_spill_count: 0
    .symbol:         _Z5k_gcnILi2EEvPKvPK15HIP_vector_typeIiLj2EEPfPKiS8_PKfPKDF16_SA_SA_SA_SA_S6_PDF16_S6_SD_SC_SA_.kd
    .uniform_work_group_size: 1
    .uses_dynamic_stack: false
    .vgpr_count:     124
    .vgpr_spill_count: 0
    .wavefront_size: 64
  - .agpr_count:     0
    .args:
      - .actual_access:  read_only
        .address_space:  global
        .offset:         0
        .size:           8
        .value_kind:     global_buffer
      - .actual_access:  read_only
        .address_space:  global
        .offset:         8
        .size:           8
        .value_kind:     global_buffer
      - .actual_access:  read_only
        .address_space:  global
        .offset:         16
        .size:           8
        .value_kind:     global_buffer
      - .actual_access:  read_only
        .address_space:  global
        .offset:         24
        .size:           8
        .value_kind:     global_buffer
      - .actual_access:  write_only
        .address_space:  global
        .offset:         32
        .size:           8
        .value_kind:     global_buffer
      - .actual_access:  read_only
        .address_space:  global
        .offset:         40
        .size:           8
        .value_kind:     global_buffer
      - .actual_access:  read_only
        .address_space:  global
        .offset:         48
        .size:           8
        .value_kind:     global_buffer
      - .actual_access:  read_only
        .address_space:  global
        .offset:         56
        .size:           8
        .value_kind:     global_buffer
      - .actual_access:  read_only
        .address_space:  global
        .offset:         64
        .size:           8
        .value_kind:     global_buffer
      - .actual_access:  read_only
        .address_space:  global
        .offset:         72
        .size:           8
        .value_kind:     global_buffer
      - .actual_access:  read_only
        .address_space:  global
        .offset:         80
        .size:           8
        .value_kind:     global_buffer
      - .actual_access:  read_only
        .address_space:  global
        .offset:         88
        .size:           8
        .value_kind:     global_buffer
      - .actual_access:  write_only
        .address_space:  global
        .offset:         96
        .size:           8
        .value_kind:     global_buffer
    .group_segment_fixed_size: 9216
    .kernarg_segment_align: 8
    .kernarg_segment_size: 104
    .language:       OpenCL C
    .language_version:
      - 2
      - 0
    .max_flat_workgroup_size: 512
    .name:           _Z6k_lstmILi256ELi10ELb1ELb0EEvPKDF16_S1_S1_PKfPDF16_S1_S1_S1_S3_S3_S3_PfS5_
    .private_segment_fixed_size: 0
    .sgpr_count:     37
    .sgpr_spill_count: 0
    .symbol:         _Z6k_lstmILi256ELi10ELb1ELb0EEvPKDF16_S1_S1_PKfPDF16_S1_S1_S1_S3_S3_S3_PfS5_.kd
    .uniform_work_group_size: 1
    .uses_dynamic_stack: false
    .vgpr_count:     256
    .vgpr_spill_count: 0
    .wavefront_size: 64
  - .agpr_count:     0
    .args:
      - .actual_access:  read_only
        .address_space:  global
        .offset:         0
        .size:           8
        .value_kind:     global_buffer
      - .actual_access:  read_only
        .address_space:  global
        .offset:         8
        .size:           8
        .value_kind:     global_buffer
      - .actual_access:  read_only
        .address_space:  global
        .offset:         16
        .size:           8
        .value_kind:     global_buffer
      - .actual_access:  read_only
        .address_space:  global
        .offset:         24
        .size:           8
        .value_kind:     global_buffer
      - .actual_access:  read_only
        .address_space:  global
        .offset:         32
        .size:           8
        .value_kind:     global_buffer
      - .actual_access:  read_only
        .address_space:  global
        .offset:         40
        .size:           8
        .value_kind:     global_buffer
      - .actual_access:  read_only
        .address_space:  global
        .offset:         48
        .size:           8
        .value_kind:     global_buffer
      - .actual_access:  read_only
        .address_space:  global
        .offset:         56
        .size:           8
        .value_kind:     global_buffer
      - .actual_access:  read_only
        .address_space:  global
        .offset:         64
        .size:           8
        .value_kind:     global_buffer
      - .actual_access:  read_only
        .address_space:  global
        .offset:         72
        .size:           8
        .value_kind:     global_buffer
      - .actual_access:  read_only
        .address_space:  global
        .offset:         80
        .size:           8
        .value_kind:     global_buffer
      - .actual_access:  write_only
        .address_space:  global
        .offset:         88
        .size:           8
        .value_kind:     global_buffer
      - .actual_access:  read_only
        .address_space:  global
        .offset:         96
        .size:           8
        .value_kind:     global_buffer
    .group_segment_fixed_size: 0
    .kernarg_segment_align: 8
    .kernarg_segment_size: 104
    .language:       OpenCL C
    .language_version:
      - 2
      - 0
    .max_flat_workgroup_size: 512
    .name:           _Z6k_lstmILi128ELi8ELb0ELb1EEvPKDF16_S1_S1_PKfPDF16_S1_S1_S1_S3_S3_S3_PfS5_
    .private_segment_fixed_size: 0
    .sgpr_count:     46
    .sgpr_spill_count: 0
    .symbol:         _Z6k_lstmILi128ELi8ELb0ELb1EEvPKDF16_S1_S1_PKfPDF16_S1_S1_S1_S3_S3_S3_PfS5_.kd
    .uniform_work_group_size: 1
    .uses_dynamic_stack: false
    .vgpr_count:     256
    .vgpr_spill_count: 0
    .wavefront_size: 64
